# fp8 GEMM K-loops (P8, P9, peeled copies too): the eight phase-1 MFMAs that hipcc sank below the phase's closing barrier go back between the phase's two s_setprio (source order), so every ping-pong int
# speedup vs baseline: 1.0097x; 1.0007x over previous
.LBB0_1549:
	s_ashr_i32 s25, s15, 31
	s_mov_b32 s24, s15
	s_lshl_b64 s[24:25], s[24:25], 19
	s_add_u32 s24, s16, s24
	s_addc_u32 s25, s17, s25
	s_and_b64 vcc, exec, s[10:11]
	s_cbranch_vccnz .LBB0_1545
	s_and_b64 s[30:31], s[26:27], exec
	s_cselect_b32 s67, s25, s29
	s_cselect_b32 s68, s24, s28
	s_lshl_b32 s30, s64, 11
	s_add_i32 s30, s30, 0
	s_add_i32 s30, s30, 0x20400
	s_add_u32 s69, s28, 0x100
	v_mov_b32_e32 v50, 0
	v_add3_u32 v179, s30, v198, v199
	v_add3_u32 v180, s30, v200, v201
	s_addc_u32 s70, s29, 0
	s_mov_b32 s71, 0
	s_mov_b64 s[28:29], 0
	ds_read_b128 v[2:5], v206
	ds_read_b128 v[10:13], v206 offset:2048
	ds_read_b128 v[6:9], v207
	ds_read_b128 v[14:17], v207 offset:2048
	s_cmp_eq_u32 s51, s71
	s_cselect_b64 s[34:35], -1, 0
	s_add_u32 s30, s53, s28
	s_addc_u32 s31, s54, s29
	s_mov_b32 m0, s55
	ds_read_b128 v[26:29], v208
	ds_read_b128 v[18:21], v208 offset:2048
	ds_read_b128 v[30:33], v209
	ds_read_b128 v[22:25], v209 offset:2048
	ds_read_b128 v[42:45], v208 offset:4096
	ds_read_b128 v[34:37], v208 offset:6144
	ds_read_b128 v[46:49], v209 offset:4096
	ds_read_b128 v[38:41], v209 offset:6144
	global_load_lds_dwordx4 v192, s[30:31]
	s_mov_b32 m0, s56
	s_nop 0
	global_load_lds_dwordx4 v194, s[30:31]
	s_waitcnt lgkmcnt(8)
	s_barrier
	s_waitcnt lgkmcnt(0)
	s_setprio 1
	v_mfma_scale_f32_16x16x128_f8f6f4 v[174:177], v[2:9], v[26:33], 0, v211, v210 op_sel_hi:[0,0,0]
	v_mfma_scale_f32_16x16x128_f8f6f4 v[170:173], v[10:17], v[26:33], 0, v211, v210 op_sel_hi:[0,0,0]
	v_mfma_scale_f32_16x16x128_f8f6f4 v[166:169], v[2:9], v[18:25], 0, v211, v210 op_sel_hi:[0,0,0]
	v_mfma_scale_f32_16x16x128_f8f6f4 v[162:165], v[10:17], v[18:25], 0, v211, v210 op_sel_hi:[0,0,0]
	v_mfma_scale_f32_16x16x128_f8f6f4 v[142:145], v[2:9], v[42:49], 0, v211, v210 op_sel_hi:[0,0,0]
	v_mfma_scale_f32_16x16x128_f8f6f4 v[130:133], v[10:17], v[42:49], 0, v211, v210 op_sel_hi:[0,0,0]
	v_mfma_scale_f32_16x16x128_f8f6f4 v[118:121], v[2:9], v[34:41], 0, v211, v210 op_sel_hi:[0,0,0]
	v_mfma_scale_f32_16x16x128_f8f6f4 v[114:117], v[10:17], v[34:41], 0, v211, v210 op_sel_hi:[0,0,0]
	s_setprio 0
	s_barrier
	s_and_b64 s[30:31], s[26:27], s[34:35]
	s_andn2_b64 vcc, exec, s[30:31]
	s_cbranch_vccnz .Lmy_pl2_1553
	ds_read2st64_b32 v[190:191], v179 offset1:2
	ds_read2st64_b32 v[192:193], v180 offset1:2
	s_waitcnt lgkmcnt(0)
	v_add_u32_e32 v184, v190, v1
	v_add_u32_e32 v190, v192, v181
	v_add_u32_e32 v192, v191, v1
	v_add_u32_e32 v194, v193, v181
.Lmy_pl2_1553:
	s_add_i32 s71, s71, 2
	s_add_u32 s30, s28, 0x100
	s_addc_u32 s31, s29, 0
	s_and_b64 s[36:37], s[34:35], exec
	s_cselect_b32 s36, 0, s30
	s_cselect_b32 s37, 0, s31
	s_add_u32 s36, s22, s36
	s_addc_u32 s37, s23, s37
	s_add_u32 s72, s69, s28
	s_addc_u32 s73, s70, s29
	s_and_b64 s[28:29], s[34:35], exec
	s_cselect_b32 s29, s67, s73
	s_cselect_b32 s28, s68, s72
	s_mov_b32 m0, s42
	v_add_u32_e32 v191, s57, v204
	v_lshl_add_u64 v[230:231], s[28:29], 0, v[188:189]
	v_add_u32_e32 v197, s57, v205
	ds_read_b128 v[214:217], v191
	ds_read_b128 v[222:225], v191 offset:2048
	ds_read_b128 v[218:221], v197
	ds_read_b128 v[226:229], v197 offset:2048
	global_load_lds_dwordx4 v[230:231], off
	v_lshl_add_u64 v[232:233], s[28:29], 0, v[186:187]
	s_mov_b32 m0, s43
	global_load_lds_dwordx4 v[232:233], off
	s_barrier
	v_mov_b32_e32 v193, v185
	v_mov_b32_e32 v195, v185
	s_setprio 1
	s_waitcnt lgkmcnt(0)
	v_mfma_scale_f32_16x16x128_f8f6f4 v[158:161], v[214:221], v[26:33], 0, v211, v210 op_sel_hi:[0,0,0]
	v_mfma_scale_f32_16x16x128_f8f6f4 v[154:157], v[222:229], v[26:33], 0, v211, v210 op_sel_hi:[0,0,0]
	ds_read_b128 v[26:29], v208 offset:18432
	ds_read_b128 v[30:33], v209 offset:18432
	v_mfma_scale_f32_16x16x128_f8f6f4 v[150:153], v[214:221], v[18:25], 0, v211, v210 op_sel_hi:[0,0,0]
	v_mfma_scale_f32_16x16x128_f8f6f4 v[146:149], v[222:229], v[18:25], 0, v211, v210 op_sel_hi:[0,0,0]
	ds_read_b128 v[18:21], v208 offset:16384
	ds_read_b128 v[22:25], v209 offset:16384
	v_mfma_scale_f32_16x16x128_f8f6f4 v[138:141], v[214:221], v[42:49], 0, v211, v210 op_sel_hi:[0,0,0]
	v_mfma_scale_f32_16x16x128_f8f6f4 v[134:137], v[222:229], v[42:49], 0, v211, v210 op_sel_hi:[0,0,0]
	ds_read_b128 v[42:45], v208 offset:22528
	ds_read_b128 v[46:49], v209 offset:22528
	v_mfma_scale_f32_16x16x128_f8f6f4 v[126:129], v[214:221], v[34:41], 0, v211, v210 op_sel_hi:[0,0,0]
	v_mfma_scale_f32_16x16x128_f8f6f4 v[122:125], v[222:229], v[34:41], 0, v211, v210 op_sel_hi:[0,0,0]
	ds_read_b128 v[34:37], v208 offset:20480
	ds_read_b128 v[38:41], v209 offset:20480
	s_setprio 0
	s_mov_b32 m0, s41
	s_barrier
	global_load_lds_dwordx4 v184, s[36:37]
	s_mov_b32 m0, s44
	v_mov_b32_e32 v191, v185
	global_load_lds_dwordx4 v190, s[36:37]
	s_barrier
	v_lshl_add_u64 v[234:235], s[36:37], 0, v[184:185]
	v_lshl_add_u64 v[236:237], s[36:37], 0, v[190:191]
	s_setprio 1
	s_waitcnt lgkmcnt(0)
	v_mfma_scale_f32_16x16x128_f8f6f4 v[110:113], v[2:9], v[18:25], 0, v211, v210 op_sel_hi:[0,0,0]
	v_mfma_scale_f32_16x16x128_f8f6f4 v[102:105], v[10:17], v[18:25], 0, v211, v210 op_sel_hi:[0,0,0]
	v_mfma_scale_f32_16x16x128_f8f6f4 v[94:97], v[2:9], v[26:33], 0, v211, v210 op_sel_hi:[0,0,0]
	v_mfma_scale_f32_16x16x128_f8f6f4 v[86:89], v[10:17], v[26:33], 0, v211, v210 op_sel_hi:[0,0,0]
	v_mfma_scale_f32_16x16x128_f8f6f4 v[78:81], v[2:9], v[34:41], 0, v211, v210 op_sel_hi:[0,0,0]
	v_mfma_scale_f32_16x16x128_f8f6f4 v[70:73], v[10:17], v[34:41], 0, v211, v210 op_sel_hi:[0,0,0]
	v_mfma_scale_f32_16x16x128_f8f6f4 v[62:65], v[2:9], v[42:49], 0, v211, v210 op_sel_hi:[0,0,0]
	v_mfma_scale_f32_16x16x128_f8f6f4 v[54:57], v[10:17], v[42:49], 0, v211, v210 op_sel_hi:[0,0,0]
	s_setprio 0
	s_barrier
	s_add_u32 s34, s28, 0x40000
	s_addc_u32 s35, s29, 0
	s_mov_b32 m0, s59
	v_lshl_add_u64 v[2:3], s[34:35], 0, v[188:189]
	global_load_lds_dwordx4 v[2:3], off
	v_lshl_add_u64 v[2:3], s[34:35], 0, v[186:187]
	s_mov_b32 m0, s60
	s_nop 0
	global_load_lds_dwordx4 v[2:3], off
	s_waitcnt vmcnt(6)
	s_barrier
	s_setprio 1
	v_mfma_scale_f32_16x16x128_f8f6f4 v[106:109], v[214:221], v[18:25], 0, v211, v210 op_sel_hi:[0,0,0]
	v_mfma_scale_f32_16x16x128_f8f6f4 v[98:101], v[222:229], v[18:25], 0, v211, v210 op_sel_hi:[0,0,0]
	ds_read_b128 v[18:21], v208 offset:32768
	ds_read_b128 v[22:25], v209 offset:32768
	v_mfma_scale_f32_16x16x128_f8f6f4 v[90:93], v[214:221], v[26:33], 0, v211, v210 op_sel_hi:[0,0,0]
	v_mfma_scale_f32_16x16x128_f8f6f4 v[82:85], v[222:229], v[26:33], 0, v211, v210 op_sel_hi:[0,0,0]
	ds_read_b128 v[26:29], v208 offset:34816
	ds_read_b128 v[30:33], v209 offset:34816
	v_mfma_scale_f32_16x16x128_f8f6f4 v[74:77], v[214:221], v[34:41], 0, v211, v210 op_sel_hi:[0,0,0]
	v_mfma_scale_f32_16x16x128_f8f6f4 v[66:69], v[222:229], v[34:41], 0, v211, v210 op_sel_hi:[0,0,0]
	ds_read_b128 v[34:37], v208 offset:36864
	ds_read_b128 v[38:41], v209 offset:36864
	v_mfma_scale_f32_16x16x128_f8f6f4 v[58:61], v[214:221], v[42:49], 0, v211, v210 op_sel_hi:[0,0,0]
	v_mfma_scale_f32_16x16x128_f8f6f4 v[50:53], v[222:229], v[42:49], 0, v211, v210 op_sel_hi:[0,0,0]
	ds_read_b128 v[42:45], v208 offset:38912
	ds_read_b128 v[46:49], v209 offset:38912
	s_setprio 0
	v_add_u32_e32 v6, s61, v204
	v_add_u32_e32 v14, s61, v205
	s_barrier
	ds_read_b128 v[2:5], v6
	ds_read_b128 v[10:13], v6 offset:2048
	ds_read_b128 v[6:9], v14
	ds_read_b128 v[14:17], v14 offset:2048
	s_mov_b32 m0, s45
	v_lshl_add_u64 v[214:215], s[36:37], 0, v[192:193]
	global_load_lds_dwordx4 v[214:215], off
	v_lshl_add_u64 v[214:215], s[36:37], 0, v[194:195]
	s_mov_b32 m0, s46
	s_nop 0
	global_load_lds_dwordx4 v[214:215], off
	s_waitcnt lgkmcnt(8)
	s_barrier
	s_setprio 1
	s_waitcnt lgkmcnt(0)
	v_mfma_scale_f32_16x16x128_f8f6f4 v[174:177], v[2:9], v[18:25], v[174:177], v211, v210 op_sel_hi:[0,0,0]
	v_mfma_scale_f32_16x16x128_f8f6f4 v[170:173], v[10:17], v[18:25], v[170:173], v211, v210 op_sel_hi:[0,0,0]
	v_mfma_scale_f32_16x16x128_f8f6f4 v[166:169], v[2:9], v[26:33], v[166:169], v211, v210 op_sel_hi:[0,0,0]
	v_mfma_scale_f32_16x16x128_f8f6f4 v[162:165], v[10:17], v[26:33], v[162:165], v211, v210 op_sel_hi:[0,0,0]
	v_mfma_scale_f32_16x16x128_f8f6f4 v[142:145], v[2:9], v[34:41], v[142:145], v211, v210 op_sel_hi:[0,0,0]
	v_mfma_scale_f32_16x16x128_f8f6f4 v[130:133], v[10:17], v[34:41], v[130:133], v211, v210 op_sel_hi:[0,0,0]
	v_mfma_scale_f32_16x16x128_f8f6f4 v[118:121], v[2:9], v[42:49], v[118:121], v211, v210 op_sel_hi:[0,0,0]
	v_mfma_scale_f32_16x16x128_f8f6f4 v[114:117], v[10:17], v[42:49], v[114:117], v211, v210 op_sel_hi:[0,0,0]
	s_setprio 0
	s_barrier
	s_mov_b32 m0, s63
	v_add_u32_e32 v191, s62, v204
	v_lshl_add_u64 v[230:231], v[230:231], 0, s[12:13]
	v_add_u32_e32 v193, s62, v205
	ds_read_b128 v[214:217], v191
	ds_read_b128 v[222:225], v191 offset:2048
	ds_read_b128 v[218:221], v193
	ds_read_b128 v[226:229], v193 offset:2048
	global_load_lds_dwordx4 v[230:231], off
	v_lshl_add_u64 v[230:231], v[232:233], 0, s[12:13]
	s_add_i32 m0, s63, 0x2000
	s_nop 0
	global_load_lds_dwordx4 v[230:231], off
	s_barrier
	s_setprio 1
	s_waitcnt lgkmcnt(0)
	v_mfma_scale_f32_16x16x128_f8f6f4 v[158:161], v[214:221], v[18:25], v[158:161], v211, v210 op_sel_hi:[0,0,0]
	v_mfma_scale_f32_16x16x128_f8f6f4 v[154:157], v[222:229], v[18:25], v[154:157], v211, v210 op_sel_hi:[0,0,0]
	ds_read_b128 v[18:21], v208 offset:49152
	ds_read_b128 v[22:25], v209 offset:49152
	v_mfma_scale_f32_16x16x128_f8f6f4 v[150:153], v[214:221], v[26:33], v[150:153], v211, v210 op_sel_hi:[0,0,0]
	v_mfma_scale_f32_16x16x128_f8f6f4 v[146:149], v[222:229], v[26:33], v[146:149], v211, v210 op_sel_hi:[0,0,0]
	ds_read_b128 v[26:29], v208 offset:51200
	ds_read_b128 v[30:33], v209 offset:51200
	v_mfma_scale_f32_16x16x128_f8f6f4 v[138:141], v[214:221], v[34:41], v[138:141], v211, v210 op_sel_hi:[0,0,0]
	v_mfma_scale_f32_16x16x128_f8f6f4 v[134:137], v[222:229], v[34:41], v[134:137], v211, v210 op_sel_hi:[0,0,0]
	ds_read_b128 v[34:37], v208 offset:53248
	ds_read_b128 v[38:41], v209 offset:53248
	v_mfma_scale_f32_16x16x128_f8f6f4 v[126:129], v[214:221], v[42:49], v[126:129], v211, v210 op_sel_hi:[0,0,0]
	v_mfma_scale_f32_16x16x128_f8f6f4 v[122:125], v[222:229], v[42:49], v[122:125], v211, v210 op_sel_hi:[0,0,0]
	ds_read_b128 v[42:45], v208 offset:55296
	ds_read_b128 v[46:49], v209 offset:55296
	s_setprio 0
	s_mov_b32 m0, s49
	v_lshl_add_u64 v[230:231], v[234:235], 0, s[12:13]
	s_barrier
	global_load_lds_dwordx4 v[230:231], off
	v_lshl_add_u64 v[230:231], v[236:237], 0, s[12:13]
	s_mov_b32 m0, s50
	s_nop 0
	global_load_lds_dwordx4 v[230:231], off
	s_barrier
	s_setprio 1
	s_waitcnt lgkmcnt(0)
	v_mfma_scale_f32_16x16x128_f8f6f4 v[110:113], v[2:9], v[18:25], v[110:113], v211, v210 op_sel_hi:[0,0,0]
	v_mfma_scale_f32_16x16x128_f8f6f4 v[102:105], v[10:17], v[18:25], v[102:105], v211, v210 op_sel_hi:[0,0,0]
	v_mfma_scale_f32_16x16x128_f8f6f4 v[94:97], v[2:9], v[26:33], v[94:97], v211, v210 op_sel_hi:[0,0,0]
	v_mfma_scale_f32_16x16x128_f8f6f4 v[86:89], v[10:17], v[26:33], v[86:89], v211, v210 op_sel_hi:[0,0,0]
	v_mfma_scale_f32_16x16x128_f8f6f4 v[78:81], v[2:9], v[34:41], v[78:81], v211, v210 op_sel_hi:[0,0,0]
	v_mfma_scale_f32_16x16x128_f8f6f4 v[70:73], v[10:17], v[34:41], v[70:73], v211, v210 op_sel_hi:[0,0,0]
	v_mfma_scale_f32_16x16x128_f8f6f4 v[62:65], v[2:9], v[42:49], v[62:65], v211, v210 op_sel_hi:[0,0,0]
	v_mfma_scale_f32_16x16x128_f8f6f4 v[54:57], v[10:17], v[42:49], v[54:57], v211, v210 op_sel_hi:[0,0,0]
	s_setprio 0
	s_barrier
	s_add_u32 s28, s28, 0x40080
	s_addc_u32 s29, s29, 0
	s_add_i32 s34, s62, s40
	v_lshl_add_u64 v[2:3], s[28:29], 0, v[188:189]
	s_mov_b32 m0, s34
	s_nop 0
	global_load_lds_dwordx4 v[2:3], off
	v_lshl_add_u64 v[2:3], s[28:29], 0, v[186:187]
	s_add_i32 m0, s34, 0x2000
	s_nop 0
	global_load_lds_dwordx4 v[2:3], off
	s_waitcnt vmcnt(6)
	s_barrier
	s_setprio 1
	v_mfma_scale_f32_16x16x128_f8f6f4 v[106:109], v[214:221], v[18:25], v[106:109], v211, v210 op_sel_hi:[0,0,0]
	ds_read_b128 v[2:5], v206
	ds_read_b128 v[10:13], v206 offset:2048
	ds_read_b128 v[6:9], v207
	ds_read_b128 v[14:17], v207 offset:2048
	v_mfma_scale_f32_16x16x128_f8f6f4 v[98:101], v[222:229], v[18:25], v[98:101], v211, v210 op_sel_hi:[0,0,0]
	ds_read_b128 v[18:21], v208 offset:2048
	ds_read_b128 v[22:25], v209 offset:2048
	v_mfma_scale_f32_16x16x128_f8f6f4 v[90:93], v[214:221], v[26:33], v[90:93], v211, v210 op_sel_hi:[0,0,0]
	v_mfma_scale_f32_16x16x128_f8f6f4 v[82:85], v[222:229], v[26:33], v[82:85], v211, v210 op_sel_hi:[0,0,0]
	ds_read_b128 v[26:29], v208
	ds_read_b128 v[30:33], v209
	v_mfma_scale_f32_16x16x128_f8f6f4 v[74:77], v[214:221], v[34:41], v[74:77], v211, v210 op_sel_hi:[0,0,0]
	v_mfma_scale_f32_16x16x128_f8f6f4 v[66:69], v[222:229], v[34:41], v[66:69], v211, v210 op_sel_hi:[0,0,0]
	ds_read_b128 v[34:37], v208 offset:6144
	ds_read_b128 v[38:41], v209 offset:6144
	v_mfma_scale_f32_16x16x128_f8f6f4 v[58:61], v[214:221], v[42:49], v[58:61], v211, v210 op_sel_hi:[0,0,0]
	v_mfma_scale_f32_16x16x128_f8f6f4 v[50:53], v[222:229], v[42:49], v[50:53], v211, v210 op_sel_hi:[0,0,0]
	ds_read_b128 v[42:45], v208 offset:4096
	ds_read_b128 v[46:49], v209 offset:4096
	s_setprio 0
	s_cmp_ge_i32 s71, s39
	s_barrier
	s_cbranch_scc1 .LBB0_1546
	s_mov_b64 s[28:29], s[30:31]
	s_branch .LBB0_1551
.LBB0_1551:
	s_cmp_eq_u32 s51, s71
	s_cselect_b64 s[34:35], -1, 0
	s_add_u32 s30, s53, s28
	s_addc_u32 s31, s54, s29
	s_mov_b32 m0, s55
	global_load_lds_dwordx4 v192, s[30:31]
	s_mov_b32 m0, s56
	s_nop 0
	global_load_lds_dwordx4 v194, s[30:31]
	s_waitcnt lgkmcnt(8)
	s_barrier
	s_waitcnt lgkmcnt(0)
	s_setprio 1
	v_mfma_scale_f32_16x16x128_f8f6f4 v[174:177], v[2:9], v[26:33], v[174:177], v211, v210 op_sel_hi:[0,0,0]
	v_mfma_scale_f32_16x16x128_f8f6f4 v[170:173], v[10:17], v[26:33], v[170:173], v211, v210 op_sel_hi:[0,0,0]
	v_mfma_scale_f32_16x16x128_f8f6f4 v[166:169], v[2:9], v[18:25], v[166:169], v211, v210 op_sel_hi:[0,0,0]
	v_mfma_scale_f32_16x16x128_f8f6f4 v[162:165], v[10:17], v[18:25], v[162:165], v211, v210 op_sel_hi:[0,0,0]
	v_mfma_scale_f32_16x16x128_f8f6f4 v[142:145], v[2:9], v[42:49], v[142:145], v211, v210 op_sel_hi:[0,0,0]
	v_mfma_scale_f32_16x16x128_f8f6f4 v[130:133], v[10:17], v[42:49], v[130:133], v211, v210 op_sel_hi:[0,0,0]
	v_mfma_scale_f32_16x16x128_f8f6f4 v[118:121], v[2:9], v[34:41], v[118:121], v211, v210 op_sel_hi:[0,0,0]
	v_mfma_scale_f32_16x16x128_f8f6f4 v[114:117], v[10:17], v[34:41], v[114:117], v211, v210 op_sel_hi:[0,0,0]
	s_setprio 0
	s_barrier
	s_and_b64 s[30:31], s[26:27], s[34:35]
	s_andn2_b64 vcc, exec, s[30:31]
	s_cbranch_vccnz .LBB0_1553
	ds_read2st64_b32 v[190:191], v179 offset1:2
	ds_read2st64_b32 v[192:193], v180 offset1:2
	s_waitcnt lgkmcnt(0)
	v_add_u32_e32 v184, v190, v1
	v_add_u32_e32 v190, v192, v181
	v_add_u32_e32 v192, v191, v1
	v_add_u32_e32 v194, v193, v181
.LBB0_1553:
	s_add_i32 s71, s71, 2
	s_add_u32 s30, s28, 0x100
	s_addc_u32 s31, s29, 0
	s_and_b64 s[36:37], s[34:35], exec
	s_cselect_b32 s36, 0, s30
	s_cselect_b32 s37, 0, s31
	s_add_u32 s36, s22, s36
	s_addc_u32 s37, s23, s37
	s_add_u32 s72, s69, s28
	s_addc_u32 s73, s70, s29
	s_and_b64 s[28:29], s[34:35], exec
	s_cselect_b32 s29, s67, s73
	s_cselect_b32 s28, s68, s72
	s_mov_b32 m0, s42
	v_add_u32_e32 v191, s57, v204
	v_lshl_add_u64 v[230:231], s[28:29], 0, v[188:189]
	v_add_u32_e32 v197, s57, v205
	ds_read_b128 v[214:217], v191
	ds_read_b128 v[222:225], v191 offset:2048
	ds_read_b128 v[218:221], v197
	ds_read_b128 v[226:229], v197 offset:2048
	global_load_lds_dwordx4 v[230:231], off
	v_lshl_add_u64 v[232:233], s[28:29], 0, v[186:187]
	s_mov_b32 m0, s43
	global_load_lds_dwordx4 v[232:233], off
	s_barrier
	v_mov_b32_e32 v193, v185
	v_mov_b32_e32 v195, v185
	s_setprio 1
	s_waitcnt lgkmcnt(0)
	v_mfma_scale_f32_16x16x128_f8f6f4 v[158:161], v[214:221], v[26:33], v[158:161], v211, v210 op_sel_hi:[0,0,0]
	v_mfma_scale_f32_16x16x128_f8f6f4 v[154:157], v[222:229], v[26:33], v[154:157], v211, v210 op_sel_hi:[0,0,0]
	ds_read_b128 v[26:29], v208 offset:18432
	ds_read_b128 v[30:33], v209 offset:18432
	v_mfma_scale_f32_16x16x128_f8f6f4 v[150:153], v[214:221], v[18:25], v[150:153], v211, v210 op_sel_hi:[0,0,0]
	v_mfma_scale_f32_16x16x128_f8f6f4 v[146:149], v[222:229], v[18:25], v[146:149], v211, v210 op_sel_hi:[0,0,0]
	ds_read_b128 v[18:21], v208 offset:16384
	ds_read_b128 v[22:25], v209 offset:16384
	v_mfma_scale_f32_16x16x128_f8f6f4 v[138:141], v[214:221], v[42:49], v[138:141], v211, v210 op_sel_hi:[0,0,0]
	v_mfma_scale_f32_16x16x128_f8f6f4 v[134:137], v[222:229], v[42:49], v[134:137], v211, v210 op_sel_hi:[0,0,0]
	ds_read_b128 v[42:45], v208 offset:22528
	ds_read_b128 v[46:49], v209 offset:22528
	v_mfma_scale_f32_16x16x128_f8f6f4 v[126:129], v[214:221], v[34:41], v[126:129], v211, v210 op_sel_hi:[0,0,0]
	v_mfma_scale_f32_16x16x128_f8f6f4 v[122:125], v[222:229], v[34:41], v[122:125], v211, v210 op_sel_hi:[0,0,0]
	ds_read_b128 v[34:37], v208 offset:20480
	ds_read_b128 v[38:41], v209 offset:20480
	s_setprio 0
	s_mov_b32 m0, s41
	s_barrier
	global_load_lds_dwordx4 v184, s[36:37]
	s_mov_b32 m0, s44
	v_mov_b32_e32 v191, v185
	global_load_lds_dwordx4 v190, s[36:37]
	s_barrier
	v_lshl_add_u64 v[234:235], s[36:37], 0, v[184:185]
	v_lshl_add_u64 v[236:237], s[36:37], 0, v[190:191]
	s_setprio 1
	s_waitcnt lgkmcnt(0)
	v_mfma_scale_f32_16x16x128_f8f6f4 v[110:113], v[2:9], v[18:25], v[110:113], v211, v210 op_sel_hi:[0,0,0]
	v_mfma_scale_f32_16x16x128_f8f6f4 v[102:105], v[10:17], v[18:25], v[102:105], v211, v210 op_sel_hi:[0,0,0]
	v_mfma_scale_f32_16x16x128_f8f6f4 v[94:97], v[2:9], v[26:33], v[94:97], v211, v210 op_sel_hi:[0,0,0]
	v_mfma_scale_f32_16x16x128_f8f6f4 v[86:89], v[10:17], v[26:33], v[86:89], v211, v210 op_sel_hi:[0,0,0]
	v_mfma_scale_f32_16x16x128_f8f6f4 v[78:81], v[2:9], v[34:41], v[78:81], v211, v210 op_sel_hi:[0,0,0]
	v_mfma_scale_f32_16x16x128_f8f6f4 v[70:73], v[10:17], v[34:41], v[70:73], v211, v210 op_sel_hi:[0,0,0]
	v_mfma_scale_f32_16x16x128_f8f6f4 v[62:65], v[2:9], v[42:49], v[62:65], v211, v210 op_sel_hi:[0,0,0]
	v_mfma_scale_f32_16x16x128_f8f6f4 v[54:57], v[10:17], v[42:49], v[54:57], v211, v210 op_sel_hi:[0,0,0]
	s_setprio 0
	s_barrier
	s_add_u32 s34, s28, 0x40000
	s_addc_u32 s35, s29, 0
	s_mov_b32 m0, s59
	v_lshl_add_u64 v[2:3], s[34:35], 0, v[188:189]
	global_load_lds_dwordx4 v[2:3], off
	v_lshl_add_u64 v[2:3], s[34:35], 0, v[186:187]
	s_mov_b32 m0, s60
	s_nop 0
	global_load_lds_dwordx4 v[2:3], off
	s_waitcnt vmcnt(6)
	s_barrier
	s_setprio 1
	v_mfma_scale_f32_16x16x128_f8f6f4 v[106:109], v[214:221], v[18:25], v[106:109], v211, v210 op_sel_hi:[0,0,0]
	v_mfma_scale_f32_16x16x128_f8f6f4 v[98:101], v[222:229], v[18:25], v[98:101], v211, v210 op_sel_hi:[0,0,0]
	ds_read_b128 v[18:21], v208 offset:32768
	ds_read_b128 v[22:25], v209 offset:32768
	v_mfma_scale_f32_16x16x128_f8f6f4 v[90:93], v[214:221], v[26:33], v[90:93], v211, v210 op_sel_hi:[0,0,0]
	v_mfma_scale_f32_16x16x128_f8f6f4 v[82:85], v[222:229], v[26:33], v[82:85], v211, v210 op_sel_hi:[0,0,0]
	ds_read_b128 v[26:29], v208 offset:34816
	ds_read_b128 v[30:33], v209 offset:34816
	v_mfma_scale_f32_16x16x128_f8f6f4 v[74:77], v[214:221], v[34:41], v[74:77], v211, v210 op_sel_hi:[0,0,0]
	v_mfma_scale_f32_16x16x128_f8f6f4 v[66:69], v[222:229], v[34:41], v[66:69], v211, v210 op_sel_hi:[0,0,0]
	ds_read_b128 v[34:37], v208 offset:36864
	ds_read_b128 v[38:41], v209 offset:36864
	v_mfma_scale_f32_16x16x128_f8f6f4 v[58:61], v[214:221], v[42:49], v[58:61], v211, v210 op_sel_hi:[0,0,0]
	v_mfma_scale_f32_16x16x128_f8f6f4 v[50:53], v[222:229], v[42:49], v[50:53], v211, v210 op_sel_hi:[0,0,0]
	ds_read_b128 v[42:45], v208 offset:38912
	ds_read_b128 v[46:49], v209 offset:38912
	s_setprio 0
	v_add_u32_e32 v6, s61, v204
	v_add_u32_e32 v14, s61, v205
	s_barrier
	ds_read_b128 v[2:5], v6
	ds_read_b128 v[10:13], v6 offset:2048
	ds_read_b128 v[6:9], v14
	ds_read_b128 v[14:17], v14 offset:2048
	s_mov_b32 m0, s45
	v_lshl_add_u64 v[214:215], s[36:37], 0, v[192:193]
	global_load_lds_dwordx4 v[214:215], off
	v_lshl_add_u64 v[214:215], s[36:37], 0, v[194:195]
	s_mov_b32 m0, s46
	s_nop 0
	global_load_lds_dwordx4 v[214:215], off
	s_waitcnt lgkmcnt(8)
	s_barrier
	s_setprio 1
	s_waitcnt lgkmcnt(0)
	v_mfma_scale_f32_16x16x128_f8f6f4 v[174:177], v[2:9], v[18:25], v[174:177], v211, v210 op_sel_hi:[0,0,0]
	v_mfma_scale_f32_16x16x128_f8f6f4 v[170:173], v[10:17], v[18:25], v[170:173], v211, v210 op_sel_hi:[0,0,0]
	v_mfma_scale_f32_16x16x128_f8f6f4 v[166:169], v[2:9], v[26:33], v[166:169], v211, v210 op_sel_hi:[0,0,0]
	v_mfma_scale_f32_16x16x128_f8f6f4 v[162:165], v[10:17], v[26:33], v[162:165], v211, v210 op_sel_hi:[0,0,0]
	v_mfma_scale_f32_16x16x128_f8f6f4 v[142:145], v[2:9], v[34:41], v[142:145], v211, v210 op_sel_hi:[0,0,0]
	v_mfma_scale_f32_16x16x128_f8f6f4 v[130:133], v[10:17], v[34:41], v[130:133], v211, v210 op_sel_hi:[0,0,0]
	v_mfma_scale_f32_16x16x128_f8f6f4 v[118:121], v[2:9], v[42:49], v[118:121], v211, v210 op_sel_hi:[0,0,0]
	v_mfma_scale_f32_16x16x128_f8f6f4 v[114:117], v[10:17], v[42:49], v[114:117], v211, v210 op_sel_hi:[0,0,0]
	s_setprio 0
	s_barrier
	s_mov_b32 m0, s63
	v_add_u32_e32 v191, s62, v204
	v_lshl_add_u64 v[230:231], v[230:231], 0, s[12:13]
	v_add_u32_e32 v193, s62, v205
	ds_read_b128 v[214:217], v191
	ds_read_b128 v[222:225], v191 offset:2048
	ds_read_b128 v[218:221], v193
	ds_read_b128 v[226:229], v193 offset:2048
	global_load_lds_dwordx4 v[230:231], off
	v_lshl_add_u64 v[230:231], v[232:233], 0, s[12:13]
	s_add_i32 m0, s63, 0x2000
	s_nop 0
	global_load_lds_dwordx4 v[230:231], off
	s_barrier
	s_setprio 1
	s_waitcnt lgkmcnt(0)
	v_mfma_scale_f32_16x16x128_f8f6f4 v[158:161], v[214:221], v[18:25], v[158:161], v211, v210 op_sel_hi:[0,0,0]
	v_mfma_scale_f32_16x16x128_f8f6f4 v[154:157], v[222:229], v[18:25], v[154:157], v211, v210 op_sel_hi:[0,0,0]
	ds_read_b128 v[18:21], v208 offset:49152
	ds_read_b128 v[22:25], v209 offset:49152
	v_mfma_scale_f32_16x16x128_f8f6f4 v[150:153], v[214:221], v[26:33], v[150:153], v211, v210 op_sel_hi:[0,0,0]
	v_mfma_scale_f32_16x16x128_f8f6f4 v[146:149], v[222:229], v[26:33], v[146:149], v211, v210 op_sel_hi:[0,0,0]
	ds_read_b128 v[26:29], v208 offset:51200
	ds_read_b128 v[30:33], v209 offset:51200
	v_mfma_scale_f32_16x16x128_f8f6f4 v[138:141], v[214:221], v[34:41], v[138:141], v211, v210 op_sel_hi:[0,0,0]
	v_mfma_scale_f32_16x16x128_f8f6f4 v[134:137], v[222:229], v[34:41], v[134:137], v211, v210 op_sel_hi:[0,0,0]
	ds_read_b128 v[34:37], v208 offset:53248
	ds_read_b128 v[38:41], v209 offset:53248
	v_mfma_scale_f32_16x16x128_f8f6f4 v[126:129], v[214:221], v[42:49], v[126:129], v211, v210 op_sel_hi:[0,0,0]
	v_mfma_scale_f32_16x16x128_f8f6f4 v[122:125], v[222:229], v[42:49], v[122:125], v211, v210 op_sel_hi:[0,0,0]
	ds_read_b128 v[42:45], v208 offset:55296
	ds_read_b128 v[46:49], v209 offset:55296
	s_setprio 0
	s_mov_b32 m0, s49
	v_lshl_add_u64 v[230:231], v[234:235], 0, s[12:13]
	s_barrier
	global_load_lds_dwordx4 v[230:231], off
	v_lshl_add_u64 v[230:231], v[236:237], 0, s[12:13]
	s_mov_b32 m0, s50
	s_nop 0
	global_load_lds_dwordx4 v[230:231], off
	s_barrier
	s_setprio 1
	s_waitcnt lgkmcnt(0)
	v_mfma_scale_f32_16x16x128_f8f6f4 v[110:113], v[2:9], v[18:25], v[110:113], v211, v210 op_sel_hi:[0,0,0]
	v_mfma_scale_f32_16x16x128_f8f6f4 v[102:105], v[10:17], v[18:25], v[102:105], v211, v210 op_sel_hi:[0,0,0]
	v_mfma_scale_f32_16x16x128_f8f6f4 v[94:97], v[2:9], v[26:33], v[94:97], v211, v210 op_sel_hi:[0,0,0]
	v_mfma_scale_f32_16x16x128_f8f6f4 v[86:89], v[10:17], v[26:33], v[86:89], v211, v210 op_sel_hi:[0,0,0]
	v_mfma_scale_f32_16x16x128_f8f6f4 v[78:81], v[2:9], v[34:41], v[78:81], v211, v210 op_sel_hi:[0,0,0]
	v_mfma_scale_f32_16x16x128_f8f6f4 v[70:73], v[10:17], v[34:41], v[70:73], v211, v210 op_sel_hi:[0,0,0]
	v_mfma_scale_f32_16x16x128_f8f6f4 v[62:65], v[2:9], v[42:49], v[62:65], v211, v210 op_sel_hi:[0,0,0]
	v_mfma_scale_f32_16x16x128_f8f6f4 v[54:57], v[10:17], v[42:49], v[54:57], v211, v210 op_sel_hi:[0,0,0]
	s_setprio 0
	s_barrier
	s_add_u32 s28, s28, 0x40080
	s_addc_u32 s29, s29, 0
	s_add_i32 s34, s62, s40
	v_lshl_add_u64 v[2:3], s[28:29], 0, v[188:189]
	s_mov_b32 m0, s34
	s_nop 0
	global_load_lds_dwordx4 v[2:3], off
	v_lshl_add_u64 v[2:3], s[28:29], 0, v[186:187]
	s_add_i32 m0, s34, 0x2000
	s_nop 0
	global_load_lds_dwordx4 v[2:3], off
	s_waitcnt vmcnt(6)
	s_barrier
	s_setprio 1
	v_mfma_scale_f32_16x16x128_f8f6f4 v[106:109], v[214:221], v[18:25], v[106:109], v211, v210 op_sel_hi:[0,0,0]
	ds_read_b128 v[2:5], v206
	ds_read_b128 v[10:13], v206 offset:2048
	ds_read_b128 v[6:9], v207
	ds_read_b128 v[14:17], v207 offset:2048
	v_mfma_scale_f32_16x16x128_f8f6f4 v[98:101], v[222:229], v[18:25], v[98:101], v211, v210 op_sel_hi:[0,0,0]
	ds_read_b128 v[18:21], v208 offset:2048
	ds_read_b128 v[22:25], v209 offset:2048
	v_mfma_scale_f32_16x16x128_f8f6f4 v[90:93], v[214:221], v[26:33], v[90:93], v211, v210 op_sel_hi:[0,0,0]
	v_mfma_scale_f32_16x16x128_f8f6f4 v[82:85], v[222:229], v[26:33], v[82:85], v211, v210 op_sel_hi:[0,0,0]
	ds_read_b128 v[26:29], v208
	ds_read_b128 v[30:33], v209
	v_mfma_scale_f32_16x16x128_f8f6f4 v[74:77], v[214:221], v[34:41], v[74:77], v211, v210 op_sel_hi:[0,0,0]
	v_mfma_scale_f32_16x16x128_f8f6f4 v[66:69], v[222:229], v[34:41], v[66:69], v211, v210 op_sel_hi:[0,0,0]
	ds_read_b128 v[34:37], v208 offset:6144
	ds_read_b128 v[38:41], v209 offset:6144
	v_mfma_scale_f32_16x16x128_f8f6f4 v[58:61], v[214:221], v[42:49], v[58:61], v211, v210 op_sel_hi:[0,0,0]
	v_mfma_scale_f32_16x16x128_f8f6f4 v[50:53], v[222:229], v[42:49], v[50:53], v211, v210 op_sel_hi:[0,0,0]
	ds_read_b128 v[42:45], v208 offset:4096
	ds_read_b128 v[46:49], v209 offset:4096
	s_setprio 0
	s_cmp_ge_i32 s71, s39
	s_barrier
	s_cbranch_scc1 .LBB0_1546
	s_mov_b64 s[28:29], s[30:31]
	s_branch .LBB0_1551

.LBB0_1671:
	s_ashr_i32 s19, s17, 31
	s_mov_b32 s18, s17
	s_lshl_b64 s[18:19], s[18:19], 17
	s_add_u32 s18, s10, s18
	s_addc_u32 s19, s11, s19
	s_and_b64 vcc, exec, s[6:7]
	s_cbranch_vccnz .LBB0_1667
	s_and_b64 s[24:25], s[20:21], exec
	s_cselect_b32 s55, s19, s23
	s_cselect_b32 s56, s18, s22
	s_lshl_b32 s24, s40, 10
	s_add_i32 s24, s24, 0
	s_add_i32 s24, s24, 0x20400
	s_add_u32 s57, s22, 0x100
	v_mov_b32_e32 v50, 0
	v_add3_u32 v179, s24, v196, v197
	v_add3_u32 v180, s24, v198, v199
	s_addc_u32 s58, s23, 0
	s_mov_b32 s59, 0
	s_mov_b64 s[22:23], 0
	ds_read_b128 v[2:5], v204
	ds_read_b128 v[10:13], v204 offset:2048
	ds_read_b128 v[6:9], v205
	ds_read_b128 v[14:17], v205 offset:2048
	s_cmp_eq_u32 s41, s59
	s_cselect_b64 s[26:27], -1, 0
	s_add_u32 s24, s42, s22
	s_addc_u32 s25, s43, s23
	s_mov_b32 m0, s44
	ds_read_b128 v[26:29], v206
	ds_read_b128 v[18:21], v206 offset:2048
	ds_read_b128 v[30:33], v207
	ds_read_b128 v[22:25], v207 offset:2048
	ds_read_b128 v[42:45], v206 offset:4096
	ds_read_b128 v[34:37], v206 offset:6144
	ds_read_b128 v[46:49], v207 offset:4096
	ds_read_b128 v[38:41], v207 offset:6144
	global_load_lds_dwordx4 v192, s[24:25]
	s_mov_b32 m0, s45
	s_nop 0
	global_load_lds_dwordx4 v194, s[24:25]
	s_waitcnt lgkmcnt(8)
	s_barrier
	s_waitcnt lgkmcnt(0)
	s_setprio 1
	v_mfma_scale_f32_16x16x128_f8f6f4 v[222:225], v[2:9], v[42:49], 0, v209, v208 op_sel_hi:[0,0,0]
	v_mfma_scale_f32_16x16x128_f8f6f4 v[226:229], v[10:17], v[42:49], 0, v209, v208 op_sel_hi:[0,0,0]
	v_mfma_scale_f32_16x16x128_f8f6f4 v[174:177], v[2:9], v[26:33], 0, v209, v208 op_sel_hi:[0,0,0]
	v_mfma_scale_f32_16x16x128_f8f6f4 v[170:173], v[10:17], v[26:33], 0, v209, v208 op_sel_hi:[0,0,0]
	v_mfma_scale_f32_16x16x128_f8f6f4 v[166:169], v[2:9], v[18:25], 0, v209, v208 op_sel_hi:[0,0,0]
	v_mfma_scale_f32_16x16x128_f8f6f4 v[162:165], v[10:17], v[18:25], 0, v209, v208 op_sel_hi:[0,0,0]
	v_mfma_scale_f32_16x16x128_f8f6f4 v[134:137], v[2:9], v[34:41], 0, v209, v208 op_sel_hi:[0,0,0]
	v_mfma_scale_f32_16x16x128_f8f6f4 v[122:125], v[10:17], v[34:41], 0, v209, v208 op_sel_hi:[0,0,0]
	s_setprio 0
	s_barrier
	s_and_b64 s[24:25], s[20:21], s[26:27]
	s_andn2_b64 vcc, exec, s[24:25]
	s_cbranch_vccnz .Lmy_pl3_1675
	ds_read2st64_b32 v[190:191], v179 offset1:2
	ds_read2st64_b32 v[192:193], v180 offset1:2
	s_waitcnt lgkmcnt(0)
	v_add_u32_e32 v184, v190, v1
	v_add_u32_e32 v190, v192, v181
	v_add_u32_e32 v192, v191, v1
	v_add_u32_e32 v194, v193, v181
.Lmy_pl3_1675:
	s_add_i32 s59, s59, 2
	s_add_u32 s24, s22, 0x100
	s_addc_u32 s25, s23, 0
	s_and_b64 s[28:29], s[26:27], exec
	s_cselect_b32 s28, 0, s24
	s_cselect_b32 s29, 0, s25
	s_add_u32 s28, s12, s28
	s_addc_u32 s29, s13, s29
	s_add_u32 s60, s57, s22
	s_addc_u32 s61, s58, s23
	s_and_b64 s[22:23], s[26:27], exec
	s_cselect_b32 s23, s55, s61
	s_cselect_b32 s22, s56, s60
	s_mov_b32 m0, s5
	s_waitcnt lgkmcnt(0)
	v_lshl_add_u64 v[238:239], s[22:23], 0, v[188:189]
	v_add_u32_e32 v191, s46, v203
	v_lshl_add_u64 v[240:241], s[22:23], 0, v[186:187]
	v_mov_b32_e32 v193, v185
	v_mov_b32_e32 v195, v185
	s_nop 1
	v_add_u32_e32 v142, s46, v202
	s_nop 6
	ds_read_b128 v[138:141], v142
	ds_read_b128 v[214:217], v142 offset:2048
	ds_read_b128 v[142:145], v191
	ds_read_b128 v[218:221], v191 offset:2048
	global_load_lds_dwordx4 v[238:239], off
	s_mov_b32 m0, s31
	s_nop 0
	global_load_lds_dwordx4 v[240:241], off
	s_barrier
	s_setprio 1
	s_waitcnt lgkmcnt(0)
	v_mfma_scale_f32_16x16x128_f8f6f4 v[158:161], v[138:145], v[26:33], 0, v209, v208 op_sel_hi:[0,0,0]
	v_mfma_scale_f32_16x16x128_f8f6f4 v[154:157], v[214:221], v[26:33], 0, v209, v208 op_sel_hi:[0,0,0]
	ds_read_b128 v[26:29], v206 offset:18432
	ds_read_b128 v[30:33], v207 offset:18432
	v_mfma_scale_f32_16x16x128_f8f6f4 v[150:153], v[138:145], v[18:25], 0, v209, v208 op_sel_hi:[0,0,0]
	v_mfma_scale_f32_16x16x128_f8f6f4 v[146:149], v[214:221], v[18:25], 0, v209, v208 op_sel_hi:[0,0,0]
	ds_read_b128 v[18:21], v206 offset:16384
	ds_read_b128 v[22:25], v207 offset:16384
	v_mfma_scale_f32_16x16x128_f8f6f4 v[130:133], v[138:145], v[42:49], 0, v209, v208 op_sel_hi:[0,0,0]
	v_mfma_scale_f32_16x16x128_f8f6f4 v[126:129], v[214:221], v[42:49], 0, v209, v208 op_sel_hi:[0,0,0]
	ds_read_b128 v[42:45], v206 offset:22528
	ds_read_b128 v[46:49], v207 offset:22528
	v_mfma_scale_f32_16x16x128_f8f6f4 v[118:121], v[138:145], v[34:41], 0, v209, v208 op_sel_hi:[0,0,0]
	v_mfma_scale_f32_16x16x128_f8f6f4 v[114:117], v[214:221], v[34:41], 0, v209, v208 op_sel_hi:[0,0,0]
	ds_read_b128 v[34:37], v206 offset:20480
	ds_read_b128 v[38:41], v207 offset:20480
	s_setprio 0
	s_mov_b32 m0, s4
	s_barrier
	global_load_lds_dwordx4 v184, s[28:29]
	s_mov_b32 m0, s33
	v_mov_b32_e32 v191, v185
	global_load_lds_dwordx4 v190, s[28:29]
	s_barrier
	v_lshl_add_u64 v[242:243], s[28:29], 0, v[184:185]
	v_lshl_add_u64 v[244:245], s[28:29], 0, v[190:191]
	s_setprio 1
	s_waitcnt lgkmcnt(0)
	v_mfma_scale_f32_16x16x128_f8f6f4 v[110:113], v[2:9], v[18:25], 0, v209, v208 op_sel_hi:[0,0,0]
	v_mfma_scale_f32_16x16x128_f8f6f4 v[106:109], v[10:17], v[18:25], 0, v209, v208 op_sel_hi:[0,0,0]
	v_mfma_scale_f32_16x16x128_f8f6f4 v[102:105], v[2:9], v[26:33], 0, v209, v208 op_sel_hi:[0,0,0]
	v_mfma_scale_f32_16x16x128_f8f6f4 v[98:101], v[10:17], v[26:33], 0, v209, v208 op_sel_hi:[0,0,0]
	v_mfma_scale_f32_16x16x128_f8f6f4 v[78:81], v[2:9], v[34:41], 0, v209, v208 op_sel_hi:[0,0,0]
	v_mfma_scale_f32_16x16x128_f8f6f4 v[74:77], v[10:17], v[34:41], 0, v209, v208 op_sel_hi:[0,0,0]
	v_mfma_scale_f32_16x16x128_f8f6f4 v[70:73], v[2:9], v[42:49], 0, v209, v208 op_sel_hi:[0,0,0]
	v_mfma_scale_f32_16x16x128_f8f6f4 v[66:69], v[10:17], v[42:49], 0, v209, v208 op_sel_hi:[0,0,0]
	s_setprio 0
	s_barrier
	s_add_u32 s26, s22, 0x10000
	s_addc_u32 s27, s23, 0
	s_mov_b32 m0, s48
	v_lshl_add_u64 v[2:3], s[26:27], 0, v[188:189]
	global_load_lds_dwordx4 v[2:3], off
	v_lshl_add_u64 v[2:3], s[26:27], 0, v[186:187]
	s_mov_b32 m0, s49
	s_nop 0
	global_load_lds_dwordx4 v[2:3], off
	s_waitcnt vmcnt(6)
	s_barrier
	s_setprio 1
	v_mfma_scale_f32_16x16x128_f8f6f4 v[94:97], v[138:145], v[18:25], 0, v209, v208 op_sel_hi:[0,0,0]
	v_mfma_scale_f32_16x16x128_f8f6f4 v[90:93], v[214:221], v[18:25], 0, v209, v208 op_sel_hi:[0,0,0]
	ds_read_b128 v[18:21], v206 offset:32768
	ds_read_b128 v[22:25], v207 offset:32768
	v_mfma_scale_f32_16x16x128_f8f6f4 v[86:89], v[138:145], v[26:33], 0, v209, v208 op_sel_hi:[0,0,0]
	v_mfma_scale_f32_16x16x128_f8f6f4 v[82:85], v[214:221], v[26:33], 0, v209, v208 op_sel_hi:[0,0,0]
	ds_read_b128 v[26:29], v206 offset:34816
	ds_read_b128 v[30:33], v207 offset:34816
	v_mfma_scale_f32_16x16x128_f8f6f4 v[62:65], v[138:145], v[34:41], 0, v209, v208 op_sel_hi:[0,0,0]
	v_mfma_scale_f32_16x16x128_f8f6f4 v[58:61], v[214:221], v[34:41], 0, v209, v208 op_sel_hi:[0,0,0]
	ds_read_b128 v[34:37], v206 offset:36864
	ds_read_b128 v[38:41], v207 offset:36864
	v_mfma_scale_f32_16x16x128_f8f6f4 v[230:233], v[138:145], v[42:49], 0, v209, v208 op_sel_hi:[0,0,0]
	v_mfma_scale_f32_16x16x128_f8f6f4 v[234:237], v[214:221], v[42:49], 0, v209, v208 op_sel_hi:[0,0,0]
	ds_read_b128 v[42:45], v206 offset:38912
	ds_read_b128 v[46:49], v207 offset:38912
	s_setprio 0
	v_add_u32_e32 v6, s50, v202
	v_add_u32_e32 v14, s50, v203
	s_barrier
	ds_read_b128 v[2:5], v6
	ds_read_b128 v[10:13], v6 offset:2048
	ds_read_b128 v[6:9], v14
	ds_read_b128 v[14:17], v14 offset:2048
	s_mov_b32 m0, s34
	v_lshl_add_u64 v[50:51], s[28:29], 0, v[192:193]
	global_load_lds_dwordx4 v[50:51], off
	v_lshl_add_u64 v[50:51], s[28:29], 0, v[194:195]
	s_mov_b32 m0, s35
	s_nop 0
	global_load_lds_dwordx4 v[50:51], off
	s_waitcnt lgkmcnt(8)
	s_barrier
	s_setprio 1
	s_waitcnt lgkmcnt(0)
	v_mfma_scale_f32_16x16x128_f8f6f4 v[174:177], v[2:9], v[18:25], v[174:177], v209, v208 op_sel_hi:[0,0,0]
	v_mfma_scale_f32_16x16x128_f8f6f4 v[170:173], v[10:17], v[18:25], v[170:173], v209, v208 op_sel_hi:[0,0,0]
	v_mfma_scale_f32_16x16x128_f8f6f4 v[166:169], v[2:9], v[26:33], v[166:169], v209, v208 op_sel_hi:[0,0,0]
	v_mfma_scale_f32_16x16x128_f8f6f4 v[162:165], v[10:17], v[26:33], v[162:165], v209, v208 op_sel_hi:[0,0,0]
	v_mfma_scale_f32_16x16x128_f8f6f4 v[142:145], v[2:9], v[34:41], v[222:225], v209, v208 op_sel_hi:[0,0,0]
	v_mfma_scale_f32_16x16x128_f8f6f4 v[138:141], v[10:17], v[34:41], v[226:229], v209, v208 op_sel_hi:[0,0,0]
	v_mfma_scale_f32_16x16x128_f8f6f4 v[134:137], v[2:9], v[42:49], v[134:137], v209, v208 op_sel_hi:[0,0,0]
	v_mfma_scale_f32_16x16x128_f8f6f4 v[122:125], v[10:17], v[42:49], v[122:125], v209, v208 op_sel_hi:[0,0,0]
	s_setprio 0
	s_barrier
	s_mov_b32 m0, s52
	v_add_u32_e32 v54, s51, v202
	v_lshl_add_u64 v[222:223], v[238:239], 0, s[8:9]
	v_add_u32_e32 v191, s51, v203
	ds_read_b128 v[50:53], v54
	ds_read_b128 v[214:217], v54 offset:2048
	ds_read_b128 v[54:57], v191
	ds_read_b128 v[218:221], v191 offset:2048
	global_load_lds_dwordx4 v[222:223], off
	v_lshl_add_u64 v[222:223], v[240:241], 0, s[8:9]
	s_mov_b32 m0, s53
	s_nop 0
	global_load_lds_dwordx4 v[222:223], off
	s_barrier
	s_setprio 1
	s_waitcnt lgkmcnt(0)
	v_mfma_scale_f32_16x16x128_f8f6f4 v[158:161], v[50:57], v[18:25], v[158:161], v209, v208 op_sel_hi:[0,0,0]
	v_mfma_scale_f32_16x16x128_f8f6f4 v[154:157], v[214:221], v[18:25], v[154:157], v209, v208 op_sel_hi:[0,0,0]
	ds_read_b128 v[18:21], v206 offset:49152
	ds_read_b128 v[22:25], v207 offset:49152
	v_mfma_scale_f32_16x16x128_f8f6f4 v[150:153], v[50:57], v[26:33], v[150:153], v209, v208 op_sel_hi:[0,0,0]
	v_mfma_scale_f32_16x16x128_f8f6f4 v[146:149], v[214:221], v[26:33], v[146:149], v209, v208 op_sel_hi:[0,0,0]
	ds_read_b128 v[26:29], v206 offset:51200
	ds_read_b128 v[30:33], v207 offset:51200
	v_mfma_scale_f32_16x16x128_f8f6f4 v[130:133], v[50:57], v[34:41], v[130:133], v209, v208 op_sel_hi:[0,0,0]
	v_mfma_scale_f32_16x16x128_f8f6f4 v[126:129], v[214:221], v[34:41], v[126:129], v209, v208 op_sel_hi:[0,0,0]
	ds_read_b128 v[34:37], v206 offset:53248
	ds_read_b128 v[38:41], v207 offset:53248
	v_mfma_scale_f32_16x16x128_f8f6f4 v[118:121], v[50:57], v[42:49], v[118:121], v209, v208 op_sel_hi:[0,0,0]
	v_mfma_scale_f32_16x16x128_f8f6f4 v[114:117], v[214:221], v[42:49], v[114:117], v209, v208 op_sel_hi:[0,0,0]
	ds_read_b128 v[42:45], v206 offset:55296
	ds_read_b128 v[46:49], v207 offset:55296
	s_setprio 0
	s_mov_b32 m0, s38
	v_lshl_add_u64 v[222:223], v[242:243], 0, s[8:9]
	s_barrier
	global_load_lds_dwordx4 v[222:223], off
	v_lshl_add_u64 v[222:223], v[244:245], 0, s[8:9]
	s_mov_b32 m0, s39
	s_nop 0
	global_load_lds_dwordx4 v[222:223], off
	s_barrier
	s_setprio 1
	s_waitcnt lgkmcnt(0)
	v_mfma_scale_f32_16x16x128_f8f6f4 v[110:113], v[2:9], v[18:25], v[110:113], v209, v208 op_sel_hi:[0,0,0]
	v_mfma_scale_f32_16x16x128_f8f6f4 v[106:109], v[10:17], v[18:25], v[106:109], v209, v208 op_sel_hi:[0,0,0]
	v_mfma_scale_f32_16x16x128_f8f6f4 v[102:105], v[2:9], v[26:33], v[102:105], v209, v208 op_sel_hi:[0,0,0]
	v_mfma_scale_f32_16x16x128_f8f6f4 v[98:101], v[10:17], v[26:33], v[98:101], v209, v208 op_sel_hi:[0,0,0]
	v_mfma_scale_f32_16x16x128_f8f6f4 v[78:81], v[2:9], v[34:41], v[78:81], v209, v208 op_sel_hi:[0,0,0]
	v_mfma_scale_f32_16x16x128_f8f6f4 v[74:77], v[10:17], v[34:41], v[74:77], v209, v208 op_sel_hi:[0,0,0]
	v_mfma_scale_f32_16x16x128_f8f6f4 v[70:73], v[2:9], v[42:49], v[70:73], v209, v208 op_sel_hi:[0,0,0]
	v_mfma_scale_f32_16x16x128_f8f6f4 v[66:69], v[10:17], v[42:49], v[66:69], v209, v208 op_sel_hi:[0,0,0]
	s_setprio 0
	s_barrier
	s_add_u32 s22, s22, 0x10080
	s_addc_u32 s23, s23, 0
	s_mov_b32 m0, s54
	v_lshl_add_u64 v[2:3], s[22:23], 0, v[188:189]
	global_load_lds_dwordx4 v[2:3], off
	v_lshl_add_u64 v[2:3], s[22:23], 0, v[186:187]
	s_add_i32 m0, s54, 0x2000
	s_nop 0
	global_load_lds_dwordx4 v[2:3], off
	s_waitcnt vmcnt(6)
	s_barrier
	s_setprio 1
	v_mfma_scale_f32_16x16x128_f8f6f4 v[94:97], v[50:57], v[18:25], v[94:97], v209, v208 op_sel_hi:[0,0,0]
	ds_read_b128 v[2:5], v204
	ds_read_b128 v[10:13], v204 offset:2048
	ds_read_b128 v[6:9], v205
	ds_read_b128 v[14:17], v205 offset:2048
	v_mfma_scale_f32_16x16x128_f8f6f4 v[90:93], v[214:221], v[18:25], v[90:93], v209, v208 op_sel_hi:[0,0,0]
	ds_read_b128 v[18:21], v206 offset:2048
	ds_read_b128 v[22:25], v207 offset:2048
	v_mfma_scale_f32_16x16x128_f8f6f4 v[86:89], v[50:57], v[26:33], v[86:89], v209, v208 op_sel_hi:[0,0,0]
	v_mfma_scale_f32_16x16x128_f8f6f4 v[82:85], v[214:221], v[26:33], v[82:85], v209, v208 op_sel_hi:[0,0,0]
	ds_read_b128 v[26:29], v206
	ds_read_b128 v[30:33], v207
	v_mfma_scale_f32_16x16x128_f8f6f4 v[62:65], v[50:57], v[34:41], v[62:65], v209, v208 op_sel_hi:[0,0,0]
	v_mfma_scale_f32_16x16x128_f8f6f4 v[58:61], v[214:221], v[34:41], v[58:61], v209, v208 op_sel_hi:[0,0,0]
	ds_read_b128 v[34:37], v206 offset:6144
	ds_read_b128 v[38:41], v207 offset:6144
	v_mfma_scale_f32_16x16x128_f8f6f4 v[54:57], v[50:57], v[42:49], v[230:233], v209, v208 op_sel_hi:[0,0,0]
	v_mfma_scale_f32_16x16x128_f8f6f4 v[50:53], v[214:221], v[42:49], v[234:237], v209, v208 op_sel_hi:[0,0,0]
	ds_read_b128 v[42:45], v206 offset:4096
	ds_read_b128 v[46:49], v207 offset:4096
	s_setprio 0
	s_cmp_ge_i32 s59, s1
	s_barrier
	s_cbranch_scc1 .LBB0_1668
	s_mov_b64 s[22:23], s[24:25]
	s_branch .LBB0_1673
.LBB0_1673:
	s_cmp_eq_u32 s41, s59
	s_cselect_b64 s[26:27], -1, 0
	s_add_u32 s24, s42, s22
	s_addc_u32 s25, s43, s23
	s_mov_b32 m0, s44
	global_load_lds_dwordx4 v192, s[24:25]
	s_mov_b32 m0, s45
	s_nop 0
	global_load_lds_dwordx4 v194, s[24:25]
	s_waitcnt lgkmcnt(8)
	s_barrier
	s_waitcnt lgkmcnt(0)
	s_setprio 1
	v_mfma_scale_f32_16x16x128_f8f6f4 v[222:225], v[2:9], v[42:49], v[142:145], v209, v208 op_sel_hi:[0,0,0]
	v_mfma_scale_f32_16x16x128_f8f6f4 v[226:229], v[10:17], v[42:49], v[138:141], v209, v208 op_sel_hi:[0,0,0]
	v_mfma_scale_f32_16x16x128_f8f6f4 v[174:177], v[2:9], v[26:33], v[174:177], v209, v208 op_sel_hi:[0,0,0]
	v_mfma_scale_f32_16x16x128_f8f6f4 v[170:173], v[10:17], v[26:33], v[170:173], v209, v208 op_sel_hi:[0,0,0]
	v_mfma_scale_f32_16x16x128_f8f6f4 v[166:169], v[2:9], v[18:25], v[166:169], v209, v208 op_sel_hi:[0,0,0]
	v_mfma_scale_f32_16x16x128_f8f6f4 v[162:165], v[10:17], v[18:25], v[162:165], v209, v208 op_sel_hi:[0,0,0]
	v_mfma_scale_f32_16x16x128_f8f6f4 v[134:137], v[2:9], v[34:41], v[134:137], v209, v208 op_sel_hi:[0,0,0]
	v_mfma_scale_f32_16x16x128_f8f6f4 v[122:125], v[10:17], v[34:41], v[122:125], v209, v208 op_sel_hi:[0,0,0]
	s_setprio 0
	s_barrier
	s_and_b64 s[24:25], s[20:21], s[26:27]
	s_andn2_b64 vcc, exec, s[24:25]
	s_cbranch_vccnz .LBB0_1675
	ds_read2st64_b32 v[190:191], v179 offset1:2
	ds_read2st64_b32 v[192:193], v180 offset1:2
	s_waitcnt lgkmcnt(0)
	v_add_u32_e32 v184, v190, v1
	v_add_u32_e32 v190, v192, v181
	v_add_u32_e32 v192, v191, v1
	v_add_u32_e32 v194, v193, v181
.LBB0_1675:
	s_add_i32 s59, s59, 2
	s_add_u32 s24, s22, 0x100
	s_addc_u32 s25, s23, 0
	s_and_b64 s[28:29], s[26:27], exec
	s_cselect_b32 s28, 0, s24
	s_cselect_b32 s29, 0, s25
	s_add_u32 s28, s12, s28
	s_addc_u32 s29, s13, s29
	s_add_u32 s60, s57, s22
	s_addc_u32 s61, s58, s23
	s_and_b64 s[22:23], s[26:27], exec
	s_cselect_b32 s23, s55, s61
	s_cselect_b32 s22, s56, s60
	s_mov_b32 m0, s5
	s_waitcnt lgkmcnt(0)
	v_lshl_add_u64 v[238:239], s[22:23], 0, v[188:189]
	v_add_u32_e32 v191, s46, v203
	v_lshl_add_u64 v[240:241], s[22:23], 0, v[186:187]
	v_mov_b32_e32 v193, v185
	v_mov_b32_e32 v195, v185
	s_nop 1
	v_add_u32_e32 v142, s46, v202
	s_nop 6
	ds_read_b128 v[138:141], v142
	ds_read_b128 v[214:217], v142 offset:2048
	ds_read_b128 v[142:145], v191
	ds_read_b128 v[218:221], v191 offset:2048
	global_load_lds_dwordx4 v[238:239], off
	s_mov_b32 m0, s31
	s_nop 0
	global_load_lds_dwordx4 v[240:241], off
	s_barrier
	s_setprio 1
	s_waitcnt lgkmcnt(0)
	v_mfma_scale_f32_16x16x128_f8f6f4 v[158:161], v[138:145], v[26:33], v[158:161], v209, v208 op_sel_hi:[0,0,0]
	v_mfma_scale_f32_16x16x128_f8f6f4 v[154:157], v[214:221], v[26:33], v[154:157], v209, v208 op_sel_hi:[0,0,0]
	ds_read_b128 v[26:29], v206 offset:18432
	ds_read_b128 v[30:33], v207 offset:18432
	v_mfma_scale_f32_16x16x128_f8f6f4 v[150:153], v[138:145], v[18:25], v[150:153], v209, v208 op_sel_hi:[0,0,0]
	v_mfma_scale_f32_16x16x128_f8f6f4 v[146:149], v[214:221], v[18:25], v[146:149], v209, v208 op_sel_hi:[0,0,0]
	ds_read_b128 v[18:21], v206 offset:16384
	ds_read_b128 v[22:25], v207 offset:16384
	v_mfma_scale_f32_16x16x128_f8f6f4 v[130:133], v[138:145], v[42:49], v[130:133], v209, v208 op_sel_hi:[0,0,0]
	v_mfma_scale_f32_16x16x128_f8f6f4 v[126:129], v[214:221], v[42:49], v[126:129], v209, v208 op_sel_hi:[0,0,0]
	ds_read_b128 v[42:45], v206 offset:22528
	ds_read_b128 v[46:49], v207 offset:22528
	v_mfma_scale_f32_16x16x128_f8f6f4 v[118:121], v[138:145], v[34:41], v[118:121], v209, v208 op_sel_hi:[0,0,0]
	v_mfma_scale_f32_16x16x128_f8f6f4 v[114:117], v[214:221], v[34:41], v[114:117], v209, v208 op_sel_hi:[0,0,0]
	ds_read_b128 v[34:37], v206 offset:20480
	ds_read_b128 v[38:41], v207 offset:20480
	s_setprio 0
	s_mov_b32 m0, s4
	s_barrier
	global_load_lds_dwordx4 v184, s[28:29]
	s_mov_b32 m0, s33
	v_mov_b32_e32 v191, v185
	global_load_lds_dwordx4 v190, s[28:29]
	s_barrier
	v_lshl_add_u64 v[242:243], s[28:29], 0, v[184:185]
	v_lshl_add_u64 v[244:245], s[28:29], 0, v[190:191]
	s_setprio 1
	s_waitcnt lgkmcnt(0)
	v_mfma_scale_f32_16x16x128_f8f6f4 v[110:113], v[2:9], v[18:25], v[110:113], v209, v208 op_sel_hi:[0,0,0]
	v_mfma_scale_f32_16x16x128_f8f6f4 v[106:109], v[10:17], v[18:25], v[106:109], v209, v208 op_sel_hi:[0,0,0]
	v_mfma_scale_f32_16x16x128_f8f6f4 v[102:105], v[2:9], v[26:33], v[102:105], v209, v208 op_sel_hi:[0,0,0]
	v_mfma_scale_f32_16x16x128_f8f6f4 v[98:101], v[10:17], v[26:33], v[98:101], v209, v208 op_sel_hi:[0,0,0]
	v_mfma_scale_f32_16x16x128_f8f6f4 v[78:81], v[2:9], v[34:41], v[78:81], v209, v208 op_sel_hi:[0,0,0]
	v_mfma_scale_f32_16x16x128_f8f6f4 v[74:77], v[10:17], v[34:41], v[74:77], v209, v208 op_sel_hi:[0,0,0]
	v_mfma_scale_f32_16x16x128_f8f6f4 v[70:73], v[2:9], v[42:49], v[70:73], v209, v208 op_sel_hi:[0,0,0]
	v_mfma_scale_f32_16x16x128_f8f6f4 v[66:69], v[10:17], v[42:49], v[66:69], v209, v208 op_sel_hi:[0,0,0]
	s_setprio 0
	s_barrier
	s_add_u32 s26, s22, 0x10000
	s_addc_u32 s27, s23, 0
	s_mov_b32 m0, s48
	v_lshl_add_u64 v[2:3], s[26:27], 0, v[188:189]
	global_load_lds_dwordx4 v[2:3], off
	v_lshl_add_u64 v[2:3], s[26:27], 0, v[186:187]
	s_mov_b32 m0, s49
	s_nop 0
	global_load_lds_dwordx4 v[2:3], off
	s_waitcnt vmcnt(6)
	s_barrier
	s_setprio 1
	v_mfma_scale_f32_16x16x128_f8f6f4 v[94:97], v[138:145], v[18:25], v[94:97], v209, v208 op_sel_hi:[0,0,0]
	v_mfma_scale_f32_16x16x128_f8f6f4 v[90:93], v[214:221], v[18:25], v[90:93], v209, v208 op_sel_hi:[0,0,0]
	ds_read_b128 v[18:21], v206 offset:32768
	ds_read_b128 v[22:25], v207 offset:32768
	v_mfma_scale_f32_16x16x128_f8f6f4 v[86:89], v[138:145], v[26:33], v[86:89], v209, v208 op_sel_hi:[0,0,0]
	v_mfma_scale_f32_16x16x128_f8f6f4 v[82:85], v[214:221], v[26:33], v[82:85], v209, v208 op_sel_hi:[0,0,0]
	ds_read_b128 v[26:29], v206 offset:34816
	ds_read_b128 v[30:33], v207 offset:34816
	v_mfma_scale_f32_16x16x128_f8f6f4 v[62:65], v[138:145], v[34:41], v[62:65], v209, v208 op_sel_hi:[0,0,0]
	v_mfma_scale_f32_16x16x128_f8f6f4 v[58:61], v[214:221], v[34:41], v[58:61], v209, v208 op_sel_hi:[0,0,0]
	ds_read_b128 v[34:37], v206 offset:36864
	ds_read_b128 v[38:41], v207 offset:36864
	v_mfma_scale_f32_16x16x128_f8f6f4 v[230:233], v[138:145], v[42:49], v[54:57], v209, v208 op_sel_hi:[0,0,0]
	v_mfma_scale_f32_16x16x128_f8f6f4 v[234:237], v[214:221], v[42:49], v[50:53], v209, v208 op_sel_hi:[0,0,0]
	ds_read_b128 v[42:45], v206 offset:38912
	ds_read_b128 v[46:49], v207 offset:38912
	s_setprio 0
	v_add_u32_e32 v6, s50, v202
	v_add_u32_e32 v14, s50, v203
	s_barrier
	ds_read_b128 v[2:5], v6
	ds_read_b128 v[10:13], v6 offset:2048
	ds_read_b128 v[6:9], v14
	ds_read_b128 v[14:17], v14 offset:2048
	s_mov_b32 m0, s34
	v_lshl_add_u64 v[50:51], s[28:29], 0, v[192:193]
	global_load_lds_dwordx4 v[50:51], off
	v_lshl_add_u64 v[50:51], s[28:29], 0, v[194:195]
	s_mov_b32 m0, s35
	s_nop 0
	global_load_lds_dwordx4 v[50:51], off
	s_waitcnt lgkmcnt(8)
	s_barrier
	s_setprio 1
	s_waitcnt lgkmcnt(0)
	v_mfma_scale_f32_16x16x128_f8f6f4 v[174:177], v[2:9], v[18:25], v[174:177], v209, v208 op_sel_hi:[0,0,0]
	v_mfma_scale_f32_16x16x128_f8f6f4 v[170:173], v[10:17], v[18:25], v[170:173], v209, v208 op_sel_hi:[0,0,0]
	v_mfma_scale_f32_16x16x128_f8f6f4 v[166:169], v[2:9], v[26:33], v[166:169], v209, v208 op_sel_hi:[0,0,0]
	v_mfma_scale_f32_16x16x128_f8f6f4 v[162:165], v[10:17], v[26:33], v[162:165], v209, v208 op_sel_hi:[0,0,0]
	v_mfma_scale_f32_16x16x128_f8f6f4 v[142:145], v[2:9], v[34:41], v[222:225], v209, v208 op_sel_hi:[0,0,0]
	v_mfma_scale_f32_16x16x128_f8f6f4 v[138:141], v[10:17], v[34:41], v[226:229], v209, v208 op_sel_hi:[0,0,0]
	v_mfma_scale_f32_16x16x128_f8f6f4 v[134:137], v[2:9], v[42:49], v[134:137], v209, v208 op_sel_hi:[0,0,0]
	v_mfma_scale_f32_16x16x128_f8f6f4 v[122:125], v[10:17], v[42:49], v[122:125], v209, v208 op_sel_hi:[0,0,0]
	s_setprio 0
	s_barrier
	s_mov_b32 m0, s52
	v_add_u32_e32 v54, s51, v202
	v_lshl_add_u64 v[222:223], v[238:239], 0, s[8:9]
	v_add_u32_e32 v191, s51, v203
	ds_read_b128 v[50:53], v54
	ds_read_b128 v[214:217], v54 offset:2048
	ds_read_b128 v[54:57], v191
	ds_read_b128 v[218:221], v191 offset:2048
	global_load_lds_dwordx4 v[222:223], off
	v_lshl_add_u64 v[222:223], v[240:241], 0, s[8:9]
	s_mov_b32 m0, s53
	s_nop 0
	global_load_lds_dwordx4 v[222:223], off
	s_barrier
	s_setprio 1
	s_waitcnt lgkmcnt(0)
	v_mfma_scale_f32_16x16x128_f8f6f4 v[158:161], v[50:57], v[18:25], v[158:161], v209, v208 op_sel_hi:[0,0,0]
	v_mfma_scale_f32_16x16x128_f8f6f4 v[154:157], v[214:221], v[18:25], v[154:157], v209, v208 op_sel_hi:[0,0,0]
	ds_read_b128 v[18:21], v206 offset:49152
	ds_read_b128 v[22:25], v207 offset:49152
	v_mfma_scale_f32_16x16x128_f8f6f4 v[150:153], v[50:57], v[26:33], v[150:153], v209, v208 op_sel_hi:[0,0,0]
	v_mfma_scale_f32_16x16x128_f8f6f4 v[146:149], v[214:221], v[26:33], v[146:149], v209, v208 op_sel_hi:[0,0,0]
	ds_read_b128 v[26:29], v206 offset:51200
	ds_read_b128 v[30:33], v207 offset:51200
	v_mfma_scale_f32_16x16x128_f8f6f4 v[130:133], v[50:57], v[34:41], v[130:133], v209, v208 op_sel_hi:[0,0,0]
	v_mfma_scale_f32_16x16x128_f8f6f4 v[126:129], v[214:221], v[34:41], v[126:129], v209, v208 op_sel_hi:[0,0,0]
	ds_read_b128 v[34:37], v206 offset:53248
	ds_read_b128 v[38:41], v207 offset:53248
	v_mfma_scale_f32_16x16x128_f8f6f4 v[118:121], v[50:57], v[42:49], v[118:121], v209, v208 op_sel_hi:[0,0,0]
	v_mfma_scale_f32_16x16x128_f8f6f4 v[114:117], v[214:221], v[42:49], v[114:117], v209, v208 op_sel_hi:[0,0,0]
	ds_read_b128 v[42:45], v206 offset:55296
	ds_read_b128 v[46:49], v207 offset:55296
	s_setprio 0
	s_mov_b32 m0, s38
	v_lshl_add_u64 v[222:223], v[242:243], 0, s[8:9]
	s_barrier
	global_load_lds_dwordx4 v[222:223], off
	v_lshl_add_u64 v[222:223], v[244:245], 0, s[8:9]
	s_mov_b32 m0, s39
	s_nop 0
	global_load_lds_dwordx4 v[222:223], off
	s_barrier
	s_setprio 1
	s_waitcnt lgkmcnt(0)
	v_mfma_scale_f32_16x16x128_f8f6f4 v[110:113], v[2:9], v[18:25], v[110:113], v209, v208 op_sel_hi:[0,0,0]
	v_mfma_scale_f32_16x16x128_f8f6f4 v[106:109], v[10:17], v[18:25], v[106:109], v209, v208 op_sel_hi:[0,0,0]
	v_mfma_scale_f32_16x16x128_f8f6f4 v[102:105], v[2:9], v[26:33], v[102:105], v209, v208 op_sel_hi:[0,0,0]
	v_mfma_scale_f32_16x16x128_f8f6f4 v[98:101], v[10:17], v[26:33], v[98:101], v209, v208 op_sel_hi:[0,0,0]
	v_mfma_scale_f32_16x16x128_f8f6f4 v[78:81], v[2:9], v[34:41], v[78:81], v209, v208 op_sel_hi:[0,0,0]
	v_mfma_scale_f32_16x16x128_f8f6f4 v[74:77], v[10:17], v[34:41], v[74:77], v209, v208 op_sel_hi:[0,0,0]
	v_mfma_scale_f32_16x16x128_f8f6f4 v[70:73], v[2:9], v[42:49], v[70:73], v209, v208 op_sel_hi:[0,0,0]
	v_mfma_scale_f32_16x16x128_f8f6f4 v[66:69], v[10:17], v[42:49], v[66:69], v209, v208 op_sel_hi:[0,0,0]
	s_setprio 0
	s_barrier
	s_add_u32 s22, s22, 0x10080
	s_addc_u32 s23, s23, 0
	s_mov_b32 m0, s54
	v_lshl_add_u64 v[2:3], s[22:23], 0, v[188:189]
	global_load_lds_dwordx4 v[2:3], off
	v_lshl_add_u64 v[2:3], s[22:23], 0, v[186:187]
	s_add_i32 m0, s54, 0x2000
	s_nop 0
	global_load_lds_dwordx4 v[2:3], off
	s_waitcnt vmcnt(6)
	s_barrier
	s_setprio 1
	v_mfma_scale_f32_16x16x128_f8f6f4 v[94:97], v[50:57], v[18:25], v[94:97], v209, v208 op_sel_hi:[0,0,0]
	v_mfma_scale_f32_16x16x128_f8f6f4 v[90:93], v[214:221], v[18:25], v[90:93], v209, v208 op_sel_hi:[0,0,0]
	v_mfma_scale_f32_16x16x128_f8f6f4 v[86:89], v[50:57], v[26:33], v[86:89], v209, v208 op_sel_hi:[0,0,0]
	v_mfma_scale_f32_16x16x128_f8f6f4 v[82:85], v[214:221], v[26:33], v[82:85], v209, v208 op_sel_hi:[0,0,0]
	v_mfma_scale_f32_16x16x128_f8f6f4 v[62:65], v[50:57], v[34:41], v[62:65], v209, v208 op_sel_hi:[0,0,0]
	v_mfma_scale_f32_16x16x128_f8f6f4 v[58:61], v[214:221], v[34:41], v[58:61], v209, v208 op_sel_hi:[0,0,0]
	v_mfma_scale_f32_16x16x128_f8f6f4 v[54:57], v[50:57], v[42:49], v[230:233], v209, v208 op_sel_hi:[0,0,0]
	v_mfma_scale_f32_16x16x128_f8f6f4 v[50:53], v[214:221], v[42:49], v[234:237], v209, v208 op_sel_hi:[0,0,0]
	s_setprio 0
	s_cmp_ge_i32 s59, s1
	s_barrier
	s_cbranch_scc1 .LBB0_1668
	s_mov_b64 s[22:23], s[24:25]
	s_branch .LBB0_1673
